# adds: P13 final combine prefetches the next token row's x2 + slot-index loads while the current row's gathered y loads / combine / stores run
# speedup vs baseline: 1.0009x; 1.0008x over previous
.LBB0_1702:
	v_readlane_b32 s2, v254, 2
	v_readlane_b32 s3, v254, 3
	s_cmp_lt_i32 s2, 14
	s_cselect_b64 s[2:3], -1, 0
	s_and_b64 s[0:1], s[2:3], s[0:1]
	s_andn2_b64 vcc, exec, s[0:1]
	s_cbranch_vccnz .LBB0_1706
	s_lshl_b32 s0, s43, 3
	v_readlane_b32 s2, v254, 25
	s_add_i32 s2, s2, s0
	s_cmpk_gt_i32 s2, 0x1fff
	v_readlane_b32 s3, v254, 26
	s_cbranch_scc1 .LBB0_1706
	v_lshlrev_b32_e32 v32, 2, v194
	v_mov_b32_e32 v33, 0
	v_lshl_add_u64 v[34:35], s[94:95], 0, v[32:33]
	v_lshlrev_b32_e32 v32, 4, v194
	s_waitcnt vmcnt(0)
	v_lshl_add_u64 v[16:17], s[90:91], 0, v[32:33]
	s_movk_i32 s0, 0x1000
	v_add_co_u32_e32 v36, vcc, s0, v16
	global_load_dwordx4 v[0:3], v32, s[90:91]
	global_load_dwordx4 v[4:7], v32, s[90:91] offset:1024
	global_load_dwordx4 v[8:11], v32, s[90:91] offset:2048
	global_load_dwordx4 v[12:15], v32, s[90:91] offset:3072
	v_addc_co_u32_e32 v37, vcc, 0, v17, vcc
	global_load_dwordx4 v[16:19], v[36:37], off
	global_load_dwordx4 v[20:23], v[36:37], off offset:1024
	global_load_dwordx4 v[24:27], v[36:37], off offset:2048
	global_load_dwordx4 v[28:31], v[36:37], off offset:3072
	v_mbcnt_lo_u32_b32 v36, -1, 0
	v_mbcnt_hi_u32_b32 v36, -1, v36
	v_and_b32_e32 v37, 64, v36
	v_add_u32_e32 v37, 64, v37
	v_xor_b32_e32 v38, 1, v36
	v_cmp_lt_i32_e32 vcc, v38, v37
	s_add_u32 s13, s94, 0x55780400
	s_mov_b64 s[0:1], 0x659a0500
	v_cndmask_b32_e32 v38, v36, v38, vcc
	v_lshlrev_b32_e32 v62, 2, v38
	v_xor_b32_e32 v38, 2, v36
	v_cmp_lt_i32_e32 vcc, v38, v37
	v_readlane_b32 s6, v254, 25
	s_addc_u32 s14, s95, 0
	v_cndmask_b32_e32 v38, v36, v38, vcc
	v_lshlrev_b32_e32 v63, 2, v38
	v_xor_b32_e32 v38, 4, v36
	v_cmp_lt_i32_e32 vcc, v38, v37
	v_lshl_add_u64 v[34:35], v[34:35], 0, s[0:1]
	s_lshl_b32 s0, s43, 5
	v_cndmask_b32_e32 v38, v36, v38, vcc
	v_lshlrev_b32_e32 v64, 2, v38
	v_xor_b32_e32 v38, 8, v36
	v_cmp_lt_i32_e32 vcc, v38, v37
	s_lshl_b32 s1, s6, 2
	s_ashr_i32 s3, s2, 31
	v_cndmask_b32_e32 v38, v36, v38, vcc
	v_lshlrev_b32_e32 v65, 2, v38
	v_xor_b32_e32 v38, 16, v36
	v_cmp_lt_i32_e32 vcc, v38, v37
	s_lshl_b32 s4, s97, 3
	s_add_i32 s6, s0, s1
	v_cndmask_b32_e32 v38, v36, v38, vcc
	v_lshlrev_b32_e32 v66, 2, v38
	v_xor_b32_e32 v38, 32, v36
	v_cmp_lt_i32_e32 vcc, v38, v37
	s_lshl_b32 s15, s97, 5
	s_lshl_b64 s[0:1], s[2:3], 12
	v_cndmask_b32_e32 v36, v36, v38, vcc
	s_add_u32 s0, s94, s0
	v_lshlrev_b32_e32 v67, 2, v36
	v_lshlrev_b32_e32 v36, 3, v194
	v_mov_b32_e32 v37, v33
	s_addc_u32 s1, s95, s1
	v_lshl_add_u64 v[36:37], s[0:1], 0, v[36:37]
	s_mov_b64 s[0:1], 0x51710000
	s_ashr_i32 s5, s4, 31
	v_lshl_add_u64 v[36:37], v[36:37], 0, s[0:1]
	s_lshl_b64 s[8:9], s[4:5], 12
	s_lshl_b64 s[0:1], s[2:3], 13
	s_add_u32 s0, s92, s0
	s_addc_u32 s1, s93, s1
	v_lshl_add_u64 v[38:39], s[0:1], 0, v[32:33]
	s_mov_b64 s[0:1], 0x1000
	s_mov_b32 s12, 0x3d800000
	v_lshl_add_u64 v[38:39], v[38:39], 0, s[0:1]
	s_lshl_b64 s[10:11], s[4:5], 13
	s_mov_b32 s3, s12
	v_mov_b32_e32 v32, 0x358637bd
	s_mov_b32 s5, 0xf800000
	v_mov_b32_e32 v68, 0x260
	v_mov_b32_e32 v41, 0x3d800000
	v_readlane_b32 s7, v254, 26
	s_ashr_i32 s7, s6, 31
	s_lshl_b64 s[0:1], s[6:7], 2
	s_add_u32 s0, s13, s0
	s_addc_u32 s1, s14, s1
	global_load_dwordx2 v[220:221], v[36:37], off offset:2560
	global_load_dwordx2 v[222:223], v[36:37], off offset:3072
	global_load_dwordx2 v[224:225], v[36:37], off offset:3584
	global_load_dwordx2 v[226:227], v[36:37], off
	global_load_dwordx2 v[228:229], v[36:37], off offset:2048
	global_load_dwordx2 v[230:231], v[36:37], off offset:512
	global_load_dwordx2 v[232:233], v[36:37], off offset:1024
	global_load_dwordx2 v[234:235], v[36:37], off offset:1536
	global_load_dwordx4 v[236:239], v33, s[0:1]
	s_add_i32 s6, s6, s15
	v_lshl_add_u64 v[36:37], v[36:37], 0, s[8:9]
	global_load_dword v240, v33, s[0:1]
	global_load_dword v240, v33, s[0:1]
	global_load_dword v240, v33, s[0:1]
	global_load_dword v240, v33, s[0:1]
	global_load_dword v240, v33, s[0:1]
	global_load_dword v240, v33, s[0:1]
	global_load_dword v240, v33, s[0:1]
	global_load_dword v240, v33, s[0:1]
.LBB0_1705:
	s_waitcnt vmcnt(8)
	v_mov_b32_e32 v48, v220
	v_mov_b32_e32 v49, v221
	v_mov_b32_e32 v50, v222
	v_mov_b32_e32 v51, v223
	v_mov_b32_e32 v56, v224
	v_mov_b32_e32 v57, v225
	v_mov_b32_e32 v54, v226
	v_mov_b32_e32 v55, v227
	v_mov_b32_e32 v42, v228
	v_mov_b32_e32 v43, v229
	v_mov_b32_e32 v52, v230
	v_mov_b32_e32 v53, v231
	v_mov_b32_e32 v46, v232
	v_mov_b32_e32 v47, v233
	v_mov_b32_e32 v44, v234
	v_mov_b32_e32 v45, v235
	v_mov_b32_e32 v70, v236
	v_mov_b32_e32 v71, v237
	v_mov_b32_e32 v72, v238
	v_mov_b32_e32 v73, v239
	s_ashr_i32 s7, s6, 31
	s_lshl_b64 s[0:1], s[6:7], 2
	s_add_u32 s0, s13, s0
	s_addc_u32 s1, s14, s1
	global_load_dwordx2 v[220:221], v[36:37], off offset:2560
	global_load_dwordx2 v[222:223], v[36:37], off offset:3072
	global_load_dwordx2 v[224:225], v[36:37], off offset:3584
	global_load_dwordx2 v[226:227], v[36:37], off
	global_load_dwordx2 v[228:229], v[36:37], off offset:2048
	global_load_dwordx2 v[230:231], v[36:37], off offset:512
	global_load_dwordx2 v[232:233], v[36:37], off offset:1024
	global_load_dwordx2 v[234:235], v[36:37], off offset:1536
	global_load_dwordx4 v[236:239], v33, s[0:1]
	s_add_i32 s6, s6, s15
	v_lshl_add_u64 v[36:37], v[36:37], 0, s[8:9]
	v_mov_b32_e32 v59, v41
	s_add_i32 s2, s2, s4
	s_cmpk_lt_i32 s2, 0x2000
	s_nop 0
	v_lshlrev_b32_e32 v40, 16, v48
	s_nop 0
	v_lshlrev_b32_e32 v74, 16, v50
	s_nop 0
	v_lshlrev_b32_e32 v69, 16, v56
	v_and_b32_e32 v61, 0xffff0000, v56
	v_lshlrev_b32_e32 v75, 16, v57
	v_and_b32_e32 v77, 0xffff0000, v57
	s_nop 0
	v_lshlrev_b32_e32 v56, 16, v54
	v_and_b32_e32 v57, 0xffff0000, v54
	s_nop 0
	v_ashrrev_i32_e32 v87, 31, v70
	v_mov_b32_e32 v86, v70
	v_ashrrev_i32_e32 v89, 31, v71
	v_mov_b32_e32 v88, v71
	v_ashrrev_i32_e32 v71, 31, v72
	v_mov_b32_e32 v70, v72
	v_ashrrev_i32_e32 v91, 31, v73
	v_mov_b32_e32 v90, v73
	v_lshlrev_b64 v[86:87], 11, v[86:87]
	v_lshlrev_b64 v[72:73], 11, v[88:89]
	v_lshlrev_b64 v[88:89], 11, v[90:91]
	v_lshlrev_b64 v[70:71], 11, v[70:71]
	v_lshl_add_u64 v[86:87], v[34:35], 0, v[86:87]
	v_lshl_add_u64 v[72:73], v[34:35], 0, v[72:73]
	v_lshl_add_u64 v[70:71], v[34:35], 0, v[70:71]
	v_lshl_add_u64 v[88:89], v[34:35], 0, v[88:89]
	global_load_dword v60, v[86:87], off
	global_load_dword v90, v[86:87], off offset:256
	global_load_dword v92, v[86:87], off offset:512
	global_load_dword v96, v[86:87], off offset:768
	global_load_dword v100, v[86:87], off offset:1024
	global_load_dword v104, v[86:87], off offset:1280
	global_load_dword v108, v[86:87], off offset:1536
	global_load_dword v112, v[86:87], off offset:1792
	global_load_dword v116, v[72:73], off
	global_load_dword v120, v[72:73], off offset:256
	global_load_dword v124, v[72:73], off offset:512
	global_load_dword v128, v[72:73], off offset:768
	global_load_dword v132, v[72:73], off offset:1024
	global_load_dword v136, v[72:73], off offset:1280
	global_load_dword v140, v[72:73], off offset:1536
	global_load_dword v144, v[72:73], off offset:1792
	global_load_dword v148, v[70:71], off
	global_load_dword v152, v[70:71], off offset:256
	global_load_dword v156, v[70:71], off offset:512
	global_load_dword v160, v[70:71], off offset:768
	global_load_dword v164, v[70:71], off offset:1024
	global_load_dword v168, v[70:71], off offset:1280
	global_load_dword v172, v[70:71], off offset:1536
	global_load_dword v176, v[70:71], off offset:1792
	global_load_dword v180, v[88:89], off
	global_load_dword v184, v[88:89], off offset:256
	global_load_dword v188, v[88:89], off offset:512
	global_load_dword v192, v[88:89], off offset:768
	global_load_dword v196, v[88:89], off offset:1024
	global_load_dword v200, v[88:89], off offset:1280
	global_load_dword v204, v[88:89], off offset:1536
	global_load_dword v208, v[88:89], off offset:1792
	v_lshlrev_b32_e32 v78, 16, v55
	v_and_b32_e32 v79, 0xffff0000, v55
	v_lshlrev_b32_e32 v81, 16, v53
	v_lshlrev_b32_e32 v80, 16, v52
	v_and_b32_e32 v53, 0xffff0000, v53
	v_and_b32_e32 v52, 0xffff0000, v52
	v_lshlrev_b32_e32 v76, 16, v51
	v_and_b32_e32 v58, 0xffff0000, v49
	v_lshlrev_b32_e32 v83, 16, v47
	v_lshlrev_b32_e32 v82, 16, v46
	v_and_b32_e32 v47, 0xffff0000, v47
	v_and_b32_e32 v46, 0xffff0000, v46
	v_lshlrev_b32_e32 v85, 16, v45
	v_lshlrev_b32_e32 v84, 16, v44
	v_and_b32_e32 v45, 0xffff0000, v45
	v_and_b32_e32 v44, 0xffff0000, v44
	v_lshlrev_b32_e32 v54, 16, v42
	v_and_b32_e32 v55, 0xffff0000, v42
	v_and_b32_e32 v48, 0xffff0000, v48
	v_lshlrev_b32_e32 v49, 16, v49
	v_and_b32_e32 v51, 0xffff0000, v51
	v_and_b32_e32 v50, 0xffff0000, v50
	v_lshlrev_b32_e32 v42, 16, v43
	v_and_b32_e32 v43, 0xffff0000, v43
	s_waitcnt vmcnt(31)
	v_cvt_pk_f32_fp8_e32 v[70:71], v60
	s_waitcnt vmcnt(30)
	v_cvt_pk_f32_fp8_e32 v[86:87], v90
	v_cvt_pk_f32_fp8_sdwa v[88:89], v90 src0_sel:WORD_1
	v_cvt_pk_f32_fp8_sdwa v[72:73], v60 src0_sel:WORD_1
	s_waitcnt vmcnt(27)
	v_cvt_pk_f32_fp8_e32 v[98:99], v100
	s_waitcnt vmcnt(26)
	v_cvt_pk_f32_fp8_e32 v[102:103], v104
	v_cvt_pk_f32_fp8_sdwa v[104:105], v104 src0_sel:WORD_1
	s_waitcnt vmcnt(25)
	v_cvt_pk_f32_fp8_e32 v[106:107], v108
	v_cvt_pk_f32_fp8_sdwa v[108:109], v108 src0_sel:WORD_1
	s_waitcnt vmcnt(22)
	v_cvt_pk_f32_fp8_e32 v[118:119], v120
	v_cvt_pk_f32_fp8_sdwa v[120:121], v120 src0_sel:WORD_1
	v_cvt_pk_f32_fp8_e32 v[90:91], v92
	s_waitcnt vmcnt(19) lgkmcnt(0)
	v_cvt_pk_f32_fp8_e32 v[130:131], v132
	s_waitcnt vmcnt(18)
	v_cvt_pk_f32_fp8_e32 v[134:135], v136
	v_cvt_pk_f32_fp8_sdwa v[136:137], v136 src0_sel:WORD_1
	s_waitcnt vmcnt(17)
	v_cvt_pk_f32_fp8_e32 v[138:139], v140
	v_cvt_pk_f32_fp8_sdwa v[140:141], v140 src0_sel:WORD_1
	v_cvt_pk_f32_fp8_sdwa v[92:93], v92 src0_sel:WORD_1
	v_cvt_pk_f32_fp8_e32 v[94:95], v96
	v_cvt_pk_f32_fp8_sdwa v[96:97], v96 src0_sel:WORD_1
	v_cvt_pk_f32_fp8_e32 v[110:111], v112
	s_waitcnt vmcnt(11)
	v_cvt_pk_f32_fp8_e32 v[162:163], v164
	s_waitcnt vmcnt(10)
	v_cvt_pk_f32_fp8_e32 v[166:167], v168
	v_cvt_pk_f32_fp8_sdwa v[168:169], v168 src0_sel:WORD_1
	v_cvt_pk_f32_fp8_sdwa v[112:113], v112 src0_sel:WORD_1
	v_cvt_pk_f32_fp8_e32 v[114:115], v116
	v_cvt_pk_f32_fp8_sdwa v[116:117], v116 src0_sel:WORD_1
	v_cvt_pk_f32_fp8_e32 v[122:123], v124
	v_cvt_pk_f32_fp8_sdwa v[124:125], v124 src0_sel:WORD_1
	s_waitcnt vmcnt(3)
	v_cvt_pk_f32_fp8_e32 v[194:195], v196
	s_waitcnt vmcnt(2)
	v_cvt_pk_f32_fp8_e32 v[198:199], v200
	v_cvt_pk_f32_fp8_sdwa v[200:201], v200 src0_sel:WORD_1
	v_cvt_pk_f32_fp8_e32 v[150:151], v152
	v_cvt_pk_f32_fp8_sdwa v[152:153], v152 src0_sel:WORD_1
	v_cvt_pk_f32_fp8_e32 v[154:155], v156
	v_cvt_pk_f32_fp8_sdwa v[156:157], v156 src0_sel:WORD_1
	v_cvt_pk_f32_fp8_e32 v[182:183], v184
	v_cvt_pk_f32_fp8_sdwa v[184:185], v184 src0_sel:WORD_1
	v_cvt_pk_f32_fp8_e32 v[186:187], v188
	v_cvt_pk_f32_fp8_sdwa v[188:189], v188 src0_sel:WORD_1
	v_cvt_pk_f32_fp8_e32 v[126:127], v128
	v_cvt_pk_f32_fp8_sdwa v[128:129], v128 src0_sel:WORD_1
	v_cvt_pk_f32_fp8_e32 v[146:147], v148
	v_cvt_pk_f32_fp8_sdwa v[148:149], v148 src0_sel:WORD_1
	v_cvt_pk_f32_fp8_e32 v[170:171], v172
	v_cvt_pk_f32_fp8_sdwa v[172:173], v172 src0_sel:WORD_1
	s_waitcnt vmcnt(1)
	v_cvt_pk_f32_fp8_e32 v[202:203], v204
	v_cvt_pk_f32_fp8_sdwa v[204:205], v204 src0_sel:WORD_1
	v_cvt_pk_f32_fp8_e32 v[142:143], v144
	v_cvt_pk_f32_fp8_sdwa v[144:145], v144 src0_sel:WORD_1
	v_cvt_pk_f32_fp8_e32 v[158:159], v160
	v_cvt_pk_f32_fp8_sdwa v[160:161], v160 src0_sel:WORD_1
	v_cvt_pk_f32_fp8_e32 v[178:179], v180
	v_cvt_pk_f32_fp8_sdwa v[180:181], v180 src0_sel:WORD_1
	v_mov_b32_e32 v217, v88
	v_mov_b32_e32 v88, v87
	v_cvt_pk_f32_fp8_sdwa v[100:101], v100 src0_sel:WORD_1
	v_cvt_pk_f32_fp8_e32 v[174:175], v176
	v_cvt_pk_f32_fp8_sdwa v[176:177], v176 src0_sel:WORD_1
	v_fmac_f32_e32 v74, 0x3d800000, v106
	v_mov_b32_e32 v210, v98
	v_mov_b32_e32 v211, v130
	v_mov_b32_e32 v130, v99
	v_mov_b32_e32 v98, v102
	v_mov_b32_e32 v99, v134
	v_mov_b32_e32 v134, v103
	v_mov_b32_e32 v102, v104
	v_mov_b32_e32 v103, v136
	v_mov_b32_e32 v136, v105
	v_mov_b32_e32 v104, v107
	v_mov_b32_e32 v105, v139
	v_mov_b32_e32 v106, v109
	v_mov_b32_e32 v107, v141
	v_pk_fma_f32 v[56:57], v[70:71], s[12:13], v[56:57] op_sel_hi:[1,0,1]
	v_pk_fma_f32 v[70:71], v[72:73], s[12:13], v[78:79] op_sel_hi:[1,0,1]
	v_mov_b32_e32 v72, v162
	v_mov_b32_e32 v73, v194
	v_mov_b32_e32 v194, v163
	v_mov_b32_e32 v78, v167
	v_mov_b32_e32 v79, v199
	v_mov_b32_e32 v162, v168
	v_mov_b32_e32 v163, v200
	v_mov_b32_e32 v216, v86
	v_mov_b32_e32 v87, v120
	v_mov_b32_e32 v120, v119
	v_pk_fma_f32 v[52:53], v[88:89], s[12:13], v[52:53] op_sel_hi:[1,0,1]
	v_cvt_pk_f32_fp8_sdwa v[132:133], v132 src0_sel:WORD_1
	v_cvt_pk_f32_fp8_e32 v[190:191], v192
	v_cvt_pk_f32_fp8_sdwa v[192:193], v192 src0_sel:WORD_1
	v_fmac_f32_e32 v76, 0x3d800000, v108
	v_mul_f32_e32 v108, 0x3d800000, v110
	v_mov_b32_e32 v86, v118
	v_mov_b32_e32 v118, v150
	v_mov_b32_e32 v119, v152
	v_mov_b32_e32 v152, v151
	v_mov_b32_e32 v150, v182
	v_mov_b32_e32 v151, v184
	v_mov_b32_e32 v184, v183
	v_mov_b32_e32 v182, v90
	v_mov_b32_e32 v183, v92
	v_mov_b32_e32 v92, v91
	v_mov_b32_e32 v90, v122
	v_mov_b32_e32 v91, v124
	v_mov_b32_e32 v124, v123
	v_mov_b32_e32 v122, v154
	v_mov_b32_e32 v123, v156
	v_mov_b32_e32 v156, v155
	v_mov_b32_e32 v154, v186
	v_mov_b32_e32 v155, v188
	v_mov_b32_e32 v188, v187
	v_mov_b32_e32 v186, v94
	v_mov_b32_e32 v187, v96
	v_mov_b32_e32 v96, v95
	v_mov_b32_e32 v139, v112
	v_mov_b32_e32 v141, v113
	v_mov_b32_e32 v167, v111
	v_pk_mul_f32 v[110:111], v[210:211], s[12:13] op_sel_hi:[1,0]
	v_pk_mul_f32 v[112:113], v[130:131], s[12:13] op_sel_hi:[1,0]
	v_pk_mul_f32 v[98:99], v[98:99], s[12:13] op_sel_hi:[1,0]
	v_pk_mul_f32 v[130:131], v[134:135], s[12:13] op_sel_hi:[1,0]
	v_pk_mul_f32 v[102:103], v[102:103], s[12:13] op_sel_hi:[1,0]
	v_pk_mul_f32 v[134:135], v[136:137], s[12:13] op_sel_hi:[1,0]
	v_pk_mul_f32 v[104:105], v[104:105], s[12:13] op_sel_hi:[1,0]
	v_pk_mul_f32 v[106:107], v[106:107], s[12:13] op_sel_hi:[1,0]
	v_pk_fma_f32 v[56:57], v[114:115], s[12:13], v[56:57] op_sel_hi:[1,0,1]
	v_pk_fma_f32 v[70:71], v[116:117], s[12:13], v[70:71] op_sel_hi:[1,0,1]
	v_pk_mul_f32 v[72:73], v[72:73], s[12:13] op_sel_hi:[1,0]
	v_pk_mul_f32 v[114:115], v[194:195], s[12:13] op_sel_hi:[1,0]
	v_pk_mul_f32 v[78:79], v[78:79], s[12:13] op_sel_hi:[1,0]
	v_pk_mul_f32 v[116:117], v[162:163], s[12:13] op_sel_hi:[1,0]
	v_pk_fma_f32 v[80:81], v[216:217], s[12:13], v[80:81] op_sel_hi:[1,0,1]
	v_pk_fma_f32 v[52:53], v[120:121], s[12:13], v[52:53] op_sel_hi:[1,0,1]
	v_cvt_pk_f32_fp8_sdwa v[164:165], v164 src0_sel:WORD_1
	s_waitcnt vmcnt(0)
	v_cvt_pk_f32_fp8_e32 v[206:207], v208
	v_cvt_pk_f32_fp8_sdwa v[208:209], v208 src0_sel:WORD_1
	v_mov_b32_e32 v200, v169
	v_mov_b32_e32 v168, v171
	v_mov_b32_e32 v169, v203
	v_mov_b32_e32 v212, v173
	v_mov_b32_e32 v213, v205
	v_mov_b32_e32 v94, v126
	v_mov_b32_e32 v95, v128
	v_pk_fma_f32 v[82:83], v[182:183], s[12:13], v[82:83] op_sel_hi:[1,0,1]
	v_pk_fma_f32 v[46:47], v[92:93], s[12:13], v[46:47] op_sel_hi:[1,0,1]
	v_pk_fma_f32 v[84:85], v[186:187], s[12:13], v[84:85] op_sel_hi:[1,0,1]
	v_pk_fma_f32 v[44:45], v[96:97], s[12:13], v[44:45] op_sel_hi:[1,0,1]
	v_add_f32_e32 v40, v98, v40
	v_add_f32_e32 v58, v134, v58
	v_pk_fma_f32 v[56:57], v[146:147], s[12:13], v[56:57] op_sel_hi:[1,0,1]
	v_pk_fma_f32 v[70:71], v[148:149], s[12:13], v[70:71] op_sel_hi:[1,0,1]
	v_mov_b32_e32 v88, v110
	v_mov_b32_e32 v89, v112
	v_mov_b32_e32 v92, v72
	v_mov_b32_e32 v93, v114
	v_mov_b32_e32 v114, v73
	v_mov_b32_e32 v72, v130
	v_mov_b32_e32 v73, v102
	v_mov_b32_e32 v96, v78
	v_mov_b32_e32 v97, v116
	v_mov_b32_e32 v116, v79
	v_mov_b32_e32 v78, v104
	v_mov_b32_e32 v79, v106
	v_pk_fma_f32 v[80:81], v[86:87], s[12:13], v[80:81] op_sel_hi:[1,0,1]
	v_pk_fma_f32 v[52:53], v[152:153], s[12:13], v[52:53] op_sel_hi:[1,0,1]
	v_cvt_pk_f32_fp8_sdwa v[196:197], v196 src0_sel:WORD_1
	v_mul_f32_e32 v218, 0x3d800000, v142
	v_mov_b32_e32 v128, v127
	v_mov_b32_e32 v126, v158
	v_mov_b32_e32 v127, v160
	v_mov_b32_e32 v171, v144
	v_mov_b32_e32 v173, v145
	v_mov_b32_e32 v199, v143
	v_pk_mul_f32 v[136:137], v[200:201], s[12:13] op_sel_hi:[1,0]
	v_pk_mul_f32 v[142:143], v[168:169], s[12:13] op_sel_hi:[1,0]
	v_pk_mul_f32 v[144:145], v[212:213], s[12:13] op_sel_hi:[1,0]
	v_pk_fma_f32 v[74:75], v[138:139], s[12:13], v[74:75] op_sel_hi:[1,0,1]
	v_pk_fma_f32 v[76:77], v[140:141], s[12:13], v[76:77] op_sel_hi:[1,0,1]
	v_mov_b32_e32 v112, v111
	v_mov_b32_e32 v102, v131
	v_mov_b32_e32 v106, v105
	v_pk_fma_f32 v[82:83], v[90:91], s[12:13], v[82:83] op_sel_hi:[1,0,1]
	v_pk_fma_f32 v[46:47], v[124:125], s[12:13], v[46:47] op_sel_hi:[1,0,1]
	v_pk_fma_f32 v[84:85], v[94:95], s[12:13], v[84:85] op_sel_hi:[1,0,1]
	v_add_f32_e32 v60, v40, v99
	v_add_f32_e32 v40, v58, v135
	v_pk_fma_f32 v[56:57], v[178:179], s[12:13], v[56:57] op_sel_hi:[1,0,1]
	v_pk_fma_f32 v[70:71], v[180:181], s[12:13], v[70:71] op_sel_hi:[1,0,1]
	v_pk_add_f32 v[54:55], v[88:89], v[54:55]
	v_pk_add_f32 v[48:49], v[72:73], v[48:49]
	v_pk_add_f32 v[50:51], v[78:79], v[50:51]
	v_pk_fma_f32 v[72:73], v[118:119], s[12:13], v[80:81] op_sel_hi:[1,0,1]
	v_pk_fma_f32 v[52:53], v[184:185], s[12:13], v[52:53] op_sel_hi:[1,0,1]
	v_mov_b32_e32 v160, v159
	v_pk_fma_f32 v[42:43], v[100:101], s[12:13], v[42:43] op_sel_hi:[1,0,1]
	v_mov_b32_e32 v203, v176
	v_mov_b32_e32 v205, v177
	v_mov_b32_e32 v104, v142
	v_mov_b32_e32 v105, v144
	v_pk_fma_f32 v[44:45], v[128:129], s[12:13], v[44:45] op_sel_hi:[1,0,1]
	v_pk_fma_f32 v[74:75], v[170:171], s[12:13], v[74:75] op_sel_hi:[1,0,1]
	v_pk_fma_f32 v[76:77], v[172:173], s[12:13], v[76:77] op_sel_hi:[1,0,1]
	v_pk_fma_f32 v[78:79], v[122:123], s[12:13], v[82:83] op_sel_hi:[1,0,1]
	v_pk_fma_f32 v[46:47], v[156:157], s[12:13], v[46:47] op_sel_hi:[1,0,1]
	v_pk_fma_f32 v[80:81], v[126:127], s[12:13], v[84:85] op_sel_hi:[1,0,1]
	v_pk_add_f32 v[54:55], v[54:55], v[112:113]
	v_pk_add_f32 v[48:49], v[48:49], v[102:103]
	v_add_f32_e32 v83, v40, v136
	v_pk_add_f32 v[50:51], v[50:51], v[106:107]
	v_pk_fma_f32 v[72:73], v[150:151], s[12:13], v[72:73] op_sel_hi:[1,0,1]
	v_pk_fma_f32 v[60:61], v[166:167], s[12:13], v[60:61] op_sel_hi:[1,0,1]
	v_mul_f32_e32 v58, v57, v57
	v_mul_f32_e32 v82, v71, v71
	v_pk_mul_f32 v[84:85], v[52:53], v[52:53]
	v_mov_b32_e32 v159, v192
	v_mov_b32_e32 v192, v191
	v_pk_fma_f32 v[42:43], v[132:133], s[12:13], v[42:43] op_sel_hi:[1,0,1]
	v_mov_b32_e32 v144, v143
	v_pk_fma_f32 v[44:45], v[160:161], s[12:13], v[44:45] op_sel_hi:[1,0,1]
	v_pk_fma_f32 v[74:75], v[202:203], s[12:13], v[74:75] op_sel_hi:[1,0,1]
	v_pk_fma_f32 v[76:77], v[204:205], s[12:13], v[76:77] op_sel_hi:[1,0,1]
	v_pk_fma_f32 v[46:47], v[188:189], s[12:13], v[46:47] op_sel_hi:[1,0,1]
	v_pk_add_f32 v[54:55], v[54:55], v[92:93]
	v_pk_add_f32 v[48:49], v[48:49], v[96:97]
	v_add_f32_e32 v100, v83, v137
	v_pk_add_f32 v[50:51], v[50:51], v[104:105]
	v_pk_fma_f32 v[60:61], v[198:199], s[12:13], v[60:61] op_sel_hi:[1,0,1]
	v_pk_fma_f32 v[92:93], v[56:57], v[56:57], v[58:59] op_sel_hi:[1,1,0]
	v_pk_fma_f32 v[82:83], v[70:71], v[70:71], v[82:83] op_sel_hi:[1,1,0]
	v_mov_b32_e32 v98, v72
	v_mov_b32_e32 v99, v52
	v_mov_b32_e32 v52, v73
	v_pk_fma_f32 v[72:73], v[72:73], v[72:73], v[84:85]
	v_mul_f32_e32 v109, 0x3d800000, v175
	v_mul_f32_e32 v215, 0x3d800000, v208
	v_mul_f32_e32 v209, 0x3d800000, v209
	v_mov_b32_e32 v158, v190
	v_pk_fma_f32 v[42:43], v[164:165], s[12:13], v[42:43] op_sel_hi:[1,0,1]
	v_pk_fma_f32 v[78:79], v[154:155], s[12:13], v[78:79] op_sel_hi:[1,0,1]
	v_pk_fma_f32 v[44:45], v[192:193], s[12:13], v[44:45] op_sel_hi:[1,0,1]
	v_mov_b32_e32 v214, v74
	v_mov_b32_e32 v208, v76
	v_pk_mul_f32 v[86:87], v[46:47], v[46:47]
	v_pk_add_f32 v[54:55], v[54:55], v[114:115]
	v_pk_add_f32 v[48:49], v[48:49], v[116:117]
	v_pk_add_f32 v[50:51], v[50:51], v[144:145]
	v_mov_b32_e32 v93, v108
	v_mov_b32_e32 v83, v69
	v_mov_b32_e32 v108, v60
	v_pk_add_f32 v[72:73], v[72:73], v[72:73] op_sel:[0,1] op_sel_hi:[1,0]
	v_pk_fma_f32 v[42:43], v[196:197], s[12:13], v[42:43] op_sel_hi:[1,0,1]
	v_pk_fma_f32 v[80:81], v[158:159], s[12:13], v[80:81] op_sel_hi:[1,0,1]
	v_pk_mul_f32 v[88:89], v[44:45], v[44:45]
	v_pk_add_f32 v[94:95], v[74:75], v[214:215]
	v_pk_add_f32 v[96:97], v[76:77], v[208:209]
	v_mov_b32_e32 v102, v78
	v_mov_b32_e32 v103, v46
	v_mov_b32_e32 v46, v79
	v_pk_fma_f32 v[78:79], v[78:79], v[78:79], v[86:87]
	v_pk_mul_f32 v[110:111], v[48:49], v[48:49]
	v_pk_mul_f32 v[112:113], v[50:51], v[50:51]
	v_pk_add_f32 v[82:83], v[92:93], v[82:83]
	v_pk_mov_b32 v[92:93], v[54:55], v[174:175] op_sel:[1,0]
	v_pk_add_f32 v[108:109], v[60:61], v[108:109]
	v_mov_b32_e32 v73, v218
	v_mul_f32_e32 v40, v43, v43
	v_mov_b32_e32 v104, v80
	v_mov_b32_e32 v105, v44
	v_mov_b32_e32 v44, v81
	v_pk_fma_f32 v[80:81], v[80:81], v[80:81], v[88:89]
	v_pk_mul_f32 v[86:87], v[94:95], v[94:95]
	v_pk_mul_f32 v[88:89], v[96:97], v[96:97]
	v_mov_b32_e32 v96, v95
	v_pk_add_f32 v[78:79], v[78:79], v[78:79] op_sel:[0,1] op_sel_hi:[1,0]
	v_pk_mul_f32 v[94:95], v[54:55], v[54:55]
	v_pk_mul_f32 v[114:115], v[92:93], s[2:3]
	v_mov_b32_e32 v108, v111
	v_pk_fma_f32 v[110:111], v[74:75], v[74:75], v[112:113]
	v_pk_fma_f32 v[112:113], v[76:77], v[76:77], v[112:113] op_sel:[0,0,1] op_sel_hi:[1,1,0]
	v_mov_b32_e32 v75, v50
	v_mov_b32_e32 v77, v51
	v_pk_add_f32 v[50:51], v[82:83], v[72:73]
	v_mul_f32_e32 v219, 0x3d800000, v206
	v_pk_fma_f32 v[90:91], v[42:43], v[42:43], v[40:41] op_sel_hi:[1,1,0]
	v_pk_mul_f32 v[84:85], v[60:61], v[60:61]
	v_mov_b32_e32 v40, v55
	v_pk_add_f32 v[80:81], v[80:81], v[80:81] op_sel:[0,1] op_sel_hi:[1,0]
	v_mov_b32_e32 v79, v115
	v_mov_b32_e32 v95, v51
	v_mov_b32_e32 v101, v207
	v_mov_b32_e32 v91, v219
	v_mov_b32_e32 v58, v100
	v_mov_b32_e32 v206, v48
	v_mov_b32_e32 v81, v219
	v_mov_b32_e32 v85, v109
	v_pk_add_f32 v[72:73], v[50:51], v[78:79]
	v_pk_fma_f32 v[78:79], v[92:93], v[40:41], v[94:95]
	v_mov_b32_e32 v40, v48
	v_mov_b32_e32 v61, v48
	v_mov_b32_e32 v106, v49
	v_pk_fma_f32 v[58:59], v[100:101], v[58:59], v[108:109]
	v_pk_add_f32 v[72:73], v[72:73], v[80:81]
	v_pk_add_f32 v[48:49], v[78:79], v[90:91]
	v_pk_fma_f32 v[78:79], v[206:207], v[40:41], v[84:85]
	v_pk_add_f32 v[80:81], v[72:73], v[48:49]
	v_pk_mul_f32 v[48:49], v[72:73], v[48:49]
	v_pk_add_f32 v[82:83], v[78:79], v[58:59]
	v_pk_mul_f32 v[58:59], v[78:79], v[58:59]
	v_mov_b32_e32 v111, v87
	v_mov_b32_e32 v113, v89
	v_mov_b32_e32 v81, v49
	v_mov_b32_e32 v83, v59
	v_pk_add_f32 v[50:51], v[110:111], v[112:113]
	v_pk_add_f32 v[48:49], v[80:81], v[82:83]
	v_mov_b32_e32 v107, v100
	v_pk_add_f32 v[48:49], v[48:49], v[50:51]
	v_mov_b32_e32 v78, v73
	v_add_f32_e32 v40, v48, v49
	ds_bpermute_b32 v48, v62, v40
	s_waitcnt lgkmcnt(0)
	v_add_f32_e32 v40, v40, v48
	ds_bpermute_b32 v48, v63, v40
	s_waitcnt lgkmcnt(0)
	v_add_f32_e32 v40, v40, v48
	ds_bpermute_b32 v48, v64, v40
	s_waitcnt lgkmcnt(0)
	v_add_f32_e32 v40, v40, v48
	ds_bpermute_b32 v48, v65, v40
	s_waitcnt lgkmcnt(0)
	v_add_f32_e32 v40, v40, v48
	ds_bpermute_b32 v48, v66, v40
	s_waitcnt lgkmcnt(0)
	v_add_f32_e32 v40, v40, v48
	ds_bpermute_b32 v48, v67, v40
	s_waitcnt lgkmcnt(0)
	v_add_f32_e32 v40, v40, v48
	v_fmamk_f32 v40, v40, 0x3a000000, v32
	v_mul_f32_e32 v48, 0x4f800000, v40
	v_cmp_gt_f32_e32 vcc, s5, v40
	s_nop 1
	v_cndmask_b32_e32 v40, v40, v48, vcc
	v_sqrt_f32_e32 v48, v40
	s_nop 0
	v_add_u32_e32 v49, -1, v48
	v_add_u32_e32 v50, 1, v48
	v_fma_f32 v51, -v49, v48, v40
	v_fma_f32 v58, -v50, v48, v40
	v_cmp_ge_f32_e64 s[0:1], 0, v51
	s_nop 1
	v_cndmask_b32_e64 v48, v48, v49, s[0:1]
	v_cmp_lt_f32_e64 s[0:1], 0, v58
	s_nop 1
	v_cndmask_b32_e64 v48, v48, v50, s[0:1]
	v_mul_f32_e32 v49, 0x37800000, v48
	v_cndmask_b32_e32 v48, v48, v49, vcc
	v_cmp_class_f32_e32 vcc, v40, v68
	s_nop 1
	v_cndmask_b32_e32 v40, v48, v40, vcc
	v_div_scale_f32 v48, s[0:1], v40, v40, 1.0
	v_rcp_f32_e32 v50, v48
	v_div_scale_f32 v49, vcc, 1.0, v40, 1.0
	v_fma_f32 v51, -v48, v50, 1.0
	v_fmac_f32_e32 v50, v51, v50
	v_mul_f32_e32 v51, v49, v50
	v_fma_f32 v58, -v48, v51, v49
	v_fmac_f32_e32 v51, v58, v50
	v_fma_f32 v48, -v48, v51, v49
	v_div_fmas_f32 v48, v48, v50, v51
	v_div_fixup_f32 v40, v48, v40, 1.0
	v_pk_mul_f32 v[48:49], v[56:57], v[40:41] op_sel_hi:[1,0]
	v_pk_mul_f32 v[50:51], v[70:71], v[40:41] op_sel_hi:[1,0]
	v_pk_mul_f32 v[56:57], v[98:99], v[40:41] op_sel_hi:[1,0]
	v_pk_mul_f32 v[52:53], v[52:53], v[40:41] op_sel_hi:[1,0]
	v_pk_mul_f32 v[58:59], v[102:103], v[40:41] op_sel_hi:[1,0]
	v_pk_mul_f32 v[70:71], v[46:47], v[40:41] op_sel_hi:[1,0]
	v_pk_mul_f32 v[72:73], v[104:105], v[40:41] op_sel_hi:[1,0]
	v_pk_mul_f32 v[80:81], v[44:45], v[40:41] op_sel_hi:[1,0]
	v_pk_mul_f32 v[82:83], v[54:55], v[40:41] op_sel_hi:[1,0]
	v_pk_mul_f32 v[84:85], v[42:43], v[40:41] op_sel_hi:[1,0]
	v_pk_mul_f32 v[86:87], v[60:61], v[40:41] op_sel_hi:[1,0]
	v_pk_mul_f32 v[88:89], v[106:107], v[40:41] op_sel_hi:[1,0]
	v_pk_mul_f32 v[74:75], v[74:75], v[40:41] op_sel_hi:[1,0]
	v_pk_mul_f32 v[76:77], v[76:77], v[40:41] op_sel_hi:[1,0]
	v_pk_mul_f32 v[78:79], v[78:79], v[40:41] op_sel_hi:[1,0]
	v_pk_mul_f32 v[90:91], v[96:97], v[40:41] op_sel_hi:[1,0]
	v_pk_mul_f32 v[44:45], v[2:3], v[50:51]
	v_pk_mul_f32 v[42:43], v[0:1], v[48:49]
	v_pk_mul_f32 v[48:49], v[6:7], v[52:53]
	v_pk_mul_f32 v[46:47], v[4:5], v[56:57]
	v_pk_mul_f32 v[52:53], v[10:11], v[70:71]
	v_pk_mul_f32 v[50:51], v[8:9], v[58:59]
	v_pk_mul_f32 v[56:57], v[14:15], v[80:81]
	v_pk_mul_f32 v[54:55], v[12:13], v[72:73]
	v_pk_mul_f32 v[60:61], v[18:19], v[84:85]
	v_pk_mul_f32 v[58:59], v[16:17], v[82:83]
	v_pk_mul_f32 v[72:73], v[22:23], v[88:89]
	v_pk_mul_f32 v[70:71], v[20:21], v[86:87]
	v_pk_mul_f32 v[76:77], v[26:27], v[76:77]
	v_pk_mul_f32 v[74:75], v[24:25], v[74:75]
	v_pk_mul_f32 v[80:81], v[30:31], v[90:91]
	v_pk_mul_f32 v[78:79], v[28:29], v[78:79]
	global_store_dwordx4 v[38:39], v[42:45], off offset:-4096
	global_store_dwordx4 v[38:39], v[46:49], off offset:-3072
	global_store_dwordx4 v[38:39], v[50:53], off offset:-2048
	global_store_dwordx4 v[38:39], v[54:57], off offset:-1024
	global_store_dwordx4 v[38:39], v[58:61], off
	global_store_dwordx4 v[38:39], v[70:73], off offset:1024
	global_store_dwordx4 v[38:39], v[74:77], off offset:2048
	global_store_dwordx4 v[38:39], v[78:81], off offset:3072
	v_lshl_add_u64 v[38:39], v[38:39], 0, s[10:11]
	s_cbranch_scc1 .LBB0_1705
